# P2 and P6 epilogue 16-byte output stores made write-through (sc1) to shorten the following grid barriers' L2 write-back
# baseline (speedup 1.0000x reference)
.LBB0_229:
	v_lshl_or_b32 v156, s12, 8, v148
	v_lshl_add_u32 v134, s48, 8, v137
	v_ashrrev_i32_e32 v157, 31, v156
	v_mov_b64_e32 v[158:159], s[10:11]
	v_mad_i64_i32 v[160:161], s[30:31], v134, s62, v[158:159]
	v_lshlrev_b64 v[156:157], 1, v[156:157]
	v_lshl_add_u64 v[160:161], v[160:161], 0, v[156:157]
	v_cvt_pk_bf16_f32 v126, v126, v127
	v_cvt_pk_bf16_f32 v127, v128, v129
	v_cvt_pk_bf16_f32 v128, v122, v123
	v_cvt_pk_bf16_f32 v129, v124, v125
	global_store_dwordx4 v[160:161], v[126:129], off sc1
	v_cvt_pk_bf16_f32 v118, v118, v119
	v_cvt_pk_bf16_f32 v119, v120, v121
	v_cvt_pk_bf16_f32 v120, v114, v115
	v_or_b32_e32 v114, 16, v134
	v_mad_i64_i32 v[114:115], s[30:31], v114, s62, v[158:159]
	v_lshl_add_u64 v[114:115], v[114:115], 0, v[156:157]
	v_cvt_pk_bf16_f32 v121, v116, v117
	global_store_dwordx4 v[160:161], v[118:121], off offset:64 sc1
	v_cvt_pk_bf16_f32 v110, v110, v111
	v_cvt_pk_bf16_f32 v111, v112, v113
	v_cvt_pk_bf16_f32 v112, v106, v107
	v_cvt_pk_bf16_f32 v113, v108, v109
	global_store_dwordx4 v[114:115], v[110:113], off sc1
	v_cvt_pk_bf16_f32 v102, v102, v103
	v_cvt_pk_bf16_f32 v103, v104, v105
	v_cvt_pk_bf16_f32 v104, v98, v99
	v_or_b32_e32 v98, 32, v134
	v_mad_i64_i32 v[98:99], s[30:31], v98, s62, v[158:159]
	v_lshl_add_u64 v[98:99], v[98:99], 0, v[156:157]
	v_cvt_pk_bf16_f32 v105, v100, v101
	global_store_dwordx4 v[114:115], v[102:105], off offset:64 sc1
	v_cvt_pk_bf16_f32 v94, v94, v95
	v_cvt_pk_bf16_f32 v95, v96, v97
	v_cvt_pk_bf16_f32 v96, v90, v91
	v_cvt_pk_bf16_f32 v97, v92, v93
	global_store_dwordx4 v[98:99], v[94:97], off sc1
	v_cvt_pk_bf16_f32 v86, v86, v87
	v_cvt_pk_bf16_f32 v87, v88, v89
	v_cvt_pk_bf16_f32 v88, v82, v83
	v_or_b32_e32 v82, 48, v134
	v_mad_i64_i32 v[82:83], s[30:31], v82, s62, v[158:159]
	v_lshl_add_u64 v[82:83], v[82:83], 0, v[156:157]
	v_cvt_pk_bf16_f32 v89, v84, v85
	global_store_dwordx4 v[98:99], v[86:89], off offset:64 sc1
	v_cvt_pk_bf16_f32 v78, v78, v79
	v_cvt_pk_bf16_f32 v79, v80, v81
	v_cvt_pk_bf16_f32 v80, v74, v75
	v_cvt_pk_bf16_f32 v81, v76, v77
	global_store_dwordx4 v[82:83], v[78:81], off sc1
	v_cvt_pk_bf16_f32 v70, v70, v71
	v_cvt_pk_bf16_f32 v71, v72, v73
	v_cvt_pk_bf16_f32 v72, v66, v67
	v_add_u32_e32 v66, 0x80, v134
	v_mad_i64_i32 v[66:67], s[30:31], v66, s62, v[158:159]
	v_lshl_add_u64 v[66:67], v[66:67], 0, v[156:157]
	v_cvt_pk_bf16_f32 v73, v68, v69
	global_store_dwordx4 v[82:83], v[70:73], off offset:64 sc1
	v_cvt_pk_bf16_f32 v62, v62, v63
	v_cvt_pk_bf16_f32 v63, v64, v65
	v_cvt_pk_bf16_f32 v64, v58, v59
	v_cvt_pk_bf16_f32 v65, v60, v61
	global_store_dwordx4 v[66:67], v[62:65], off sc1
	v_cvt_pk_bf16_f32 v54, v54, v55
	v_cvt_pk_bf16_f32 v55, v56, v57
	v_cvt_pk_bf16_f32 v56, v50, v51
	v_add_u32_e32 v50, 0x90, v134
	v_mad_i64_i32 v[50:51], s[30:31], v50, s62, v[158:159]
	v_lshl_add_u64 v[50:51], v[50:51], 0, v[156:157]
	v_cvt_pk_bf16_f32 v57, v52, v53
	global_store_dwordx4 v[66:67], v[54:57], off offset:64 sc1
	v_cvt_pk_bf16_f32 v46, v46, v47
	v_cvt_pk_bf16_f32 v47, v48, v49
	v_cvt_pk_bf16_f32 v48, v42, v43
	v_cvt_pk_bf16_f32 v49, v44, v45
	global_store_dwordx4 v[50:51], v[46:49], off sc1
	v_cvt_pk_bf16_f32 v38, v38, v39
	v_cvt_pk_bf16_f32 v39, v40, v41
	v_cvt_pk_bf16_f32 v40, v34, v35
	v_add_u32_e32 v34, 0xa0, v134
	v_mad_i64_i32 v[34:35], s[30:31], v34, s62, v[158:159]
	v_lshl_add_u64 v[34:35], v[34:35], 0, v[156:157]
	v_cvt_pk_bf16_f32 v41, v36, v37
	global_store_dwordx4 v[50:51], v[38:41], off offset:64 sc1
	v_cvt_pk_bf16_f32 v30, v30, v31
	v_cvt_pk_bf16_f32 v31, v32, v33
	v_cvt_pk_bf16_f32 v32, v26, v27
	v_cvt_pk_bf16_f32 v33, v28, v29
	global_store_dwordx4 v[34:35], v[30:33], off sc1
	v_cvt_pk_bf16_f32 v22, v22, v23
	v_cvt_pk_bf16_f32 v23, v24, v25
	v_cvt_pk_bf16_f32 v24, v18, v19
	v_add_u32_e32 v18, 0xb0, v134
	v_mad_i64_i32 v[18:19], s[30:31], v18, s62, v[158:159]
	v_lshl_add_u64 v[18:19], v[18:19], 0, v[156:157]
	s_and_b64 vcc, exec, s[6:7]
	s_mov_b64 s[6:7], -1
	v_cvt_pk_bf16_f32 v25, v20, v21
	global_store_dwordx4 v[34:35], v[22:25], off offset:64 sc1
	v_cvt_pk_bf16_f32 v14, v14, v15
	v_cvt_pk_bf16_f32 v15, v16, v17
	v_cvt_pk_bf16_f32 v16, v10, v11
	v_cvt_pk_bf16_f32 v17, v12, v13
	global_store_dwordx4 v[18:19], v[14:17], off sc1
	v_cvt_pk_bf16_f32 v6, v6, v7
	v_cvt_pk_bf16_f32 v7, v8, v9
	v_cvt_pk_bf16_f32 v8, v2, v3
	v_cvt_pk_bf16_f32 v9, v4, v5
	global_store_dwordx4 v[18:19], v[6:9], off offset:64 sc1
	s_mov_b32 s98, 1
	s_cbranch_vccnz .LBB0_216
	s_andn2_b64 vcc, exec, s[18:19]
	s_cbranch_vccnz .LBB0_215
	s_barrier
	s_branch .LBB0_215

.LBB0_258:
	v_lshl_or_b32 v4, s6, 8, v196
	v_lshl_add_u32 v12, s59, 8, v175
	v_ashrrev_i32_e32 v5, 31, v4
	v_mov_b64_e32 v[2:3], s[10:11]
	v_mad_i64_i32 v[6:7], s[30:31], v12, s57, v[2:3]
	v_lshlrev_b64 v[4:5], 1, v[4:5]
	v_lshl_add_u64 v[10:11], v[6:7], 0, v[4:5]
	v_cvt_pk_bf16_f32 v6, v158, v159
	v_cvt_pk_bf16_f32 v7, v160, v161
	v_cvt_pk_bf16_f32 v8, v154, v155
	v_cvt_pk_bf16_f32 v9, v156, v157
	global_store_dwordx4 v[10:11], v[6:9], off sc1
	s_and_b64 vcc, exec, s[2:3]
	s_mov_b64 s[2:3], -1
	v_cvt_pk_bf16_f32 v6, v150, v151
	v_cvt_pk_bf16_f32 v7, v152, v153
	v_cvt_pk_bf16_f32 v8, v146, v147
	v_cvt_pk_bf16_f32 v9, v148, v149
	global_store_dwordx4 v[10:11], v[6:9], off offset:64 sc1
	s_nop 1
	v_or_b32_e32 v6, 16, v12
	v_mad_i64_i32 v[6:7], s[30:31], v6, s57, v[2:3]
	v_lshl_add_u64 v[10:11], v[6:7], 0, v[4:5]
	v_cvt_pk_bf16_f32 v6, v142, v143
	v_cvt_pk_bf16_f32 v7, v144, v145
	v_cvt_pk_bf16_f32 v8, v138, v139
	v_cvt_pk_bf16_f32 v9, v140, v141
	global_store_dwordx4 v[10:11], v[6:9], off sc1
	s_nop 1
	v_cvt_pk_bf16_f32 v6, v134, v135
	v_cvt_pk_bf16_f32 v7, v136, v137
	v_cvt_pk_bf16_f32 v8, v130, v131
	v_cvt_pk_bf16_f32 v9, v132, v133
	global_store_dwordx4 v[10:11], v[6:9], off offset:64 sc1
	s_nop 1
	v_or_b32_e32 v6, 32, v12
	v_mad_i64_i32 v[6:7], s[30:31], v6, s57, v[2:3]
	v_lshl_add_u64 v[10:11], v[6:7], 0, v[4:5]
	v_cvt_pk_bf16_f32 v6, v126, v127
	v_cvt_pk_bf16_f32 v7, v128, v129
	v_cvt_pk_bf16_f32 v8, v122, v123
	v_cvt_pk_bf16_f32 v9, v124, v125
	global_store_dwordx4 v[10:11], v[6:9], off sc1
	s_nop 1
	v_cvt_pk_bf16_f32 v6, v118, v119
	v_cvt_pk_bf16_f32 v7, v120, v121
	v_cvt_pk_bf16_f32 v8, v114, v115
	v_cvt_pk_bf16_f32 v9, v116, v117
	global_store_dwordx4 v[10:11], v[6:9], off offset:64 sc1
	s_nop 1
	v_or_b32_e32 v6, 48, v12
	v_mad_i64_i32 v[6:7], s[30:31], v6, s57, v[2:3]
	v_lshl_add_u64 v[10:11], v[6:7], 0, v[4:5]
	v_cvt_pk_bf16_f32 v6, v110, v111
	v_cvt_pk_bf16_f32 v7, v112, v113
	v_cvt_pk_bf16_f32 v8, v106, v107
	v_cvt_pk_bf16_f32 v9, v108, v109
	global_store_dwordx4 v[10:11], v[6:9], off sc1
	s_nop 1
	v_cvt_pk_bf16_f32 v6, v102, v103
	v_cvt_pk_bf16_f32 v7, v104, v105
	v_cvt_pk_bf16_f32 v8, v98, v99
	v_cvt_pk_bf16_f32 v9, v100, v101
	global_store_dwordx4 v[10:11], v[6:9], off offset:64 sc1
	s_nop 1
	v_add_u32_e32 v6, 0x80, v12
	v_mad_i64_i32 v[6:7], s[30:31], v6, s57, v[2:3]
	v_lshl_add_u64 v[10:11], v[6:7], 0, v[4:5]
	v_cvt_pk_bf16_f32 v6, v94, v95
	v_cvt_pk_bf16_f32 v7, v96, v97
	v_cvt_pk_bf16_f32 v8, v90, v91
	v_cvt_pk_bf16_f32 v9, v92, v93
	global_store_dwordx4 v[10:11], v[6:9], off sc1
	s_nop 1
	v_cvt_pk_bf16_f32 v6, v86, v87
	v_cvt_pk_bf16_f32 v7, v88, v89
	v_cvt_pk_bf16_f32 v8, v82, v83
	v_cvt_pk_bf16_f32 v9, v84, v85
	global_store_dwordx4 v[10:11], v[6:9], off offset:64 sc1
	s_nop 1
	v_add_u32_e32 v6, 0x90, v12
	v_mad_i64_i32 v[6:7], s[30:31], v6, s57, v[2:3]
	v_lshl_add_u64 v[10:11], v[6:7], 0, v[4:5]
	v_cvt_pk_bf16_f32 v6, v78, v79
	v_cvt_pk_bf16_f32 v7, v80, v81
	v_cvt_pk_bf16_f32 v8, v74, v75
	v_cvt_pk_bf16_f32 v9, v76, v77
	global_store_dwordx4 v[10:11], v[6:9], off sc1
	s_nop 1
	v_cvt_pk_bf16_f32 v6, v70, v71
	v_cvt_pk_bf16_f32 v7, v72, v73
	v_cvt_pk_bf16_f32 v8, v66, v67
	v_cvt_pk_bf16_f32 v9, v68, v69
	global_store_dwordx4 v[10:11], v[6:9], off offset:64 sc1
	s_nop 1
	v_add_u32_e32 v6, 0xa0, v12
	v_mad_i64_i32 v[6:7], s[30:31], v6, s57, v[2:3]
	v_lshl_add_u64 v[10:11], v[6:7], 0, v[4:5]
	v_cvt_pk_bf16_f32 v6, v62, v63
	v_cvt_pk_bf16_f32 v7, v64, v65
	v_cvt_pk_bf16_f32 v8, v58, v59
	v_cvt_pk_bf16_f32 v9, v60, v61
	global_store_dwordx4 v[10:11], v[6:9], off sc1
	s_nop 1
	v_cvt_pk_bf16_f32 v6, v54, v55
	v_cvt_pk_bf16_f32 v7, v56, v57
	v_cvt_pk_bf16_f32 v8, v50, v51
	v_cvt_pk_bf16_f32 v9, v52, v53
	global_store_dwordx4 v[10:11], v[6:9], off offset:64 sc1
	s_nop 1
	v_add_u32_e32 v6, 0xb0, v12
	v_mad_i64_i32 v[2:3], s[30:31], v6, s57, v[2:3]
	v_lshl_add_u64 v[6:7], v[2:3], 0, v[4:5]
	v_cvt_pk_bf16_f32 v2, v46, v47
	v_cvt_pk_bf16_f32 v3, v48, v49
	v_cvt_pk_bf16_f32 v4, v42, v43
	v_cvt_pk_bf16_f32 v5, v44, v45
	global_store_dwordx4 v[6:7], v[2:5], off sc1
	s_nop 1
	v_cvt_pk_bf16_f32 v2, v38, v39
	v_cvt_pk_bf16_f32 v3, v40, v41
	v_cvt_pk_bf16_f32 v4, v34, v35
	v_cvt_pk_bf16_f32 v5, v36, v37
	global_store_dwordx4 v[6:7], v[2:5], off offset:64 sc1
	s_mov_b32 s99, 1
	s_cbranch_vccnz .LBB0_244
	s_andn2_b64 vcc, exec, s[16:17]
	s_cbranch_vccnz .LBB0_243
	s_barrier
	s_branch .LBB0_243

.LBB0_1077:
	v_lshl_or_b32 v164, s65, 8, v167
	v_ashrrev_i32_e32 v165, 31, v164
	v_lshl_add_u64 v[130:131], v[164:165], 2, s[14:15]
	global_load_dwordx4 v[142:145], v[130:131], off
	global_load_dwordx4 v[138:141], v[130:131], off offset:16
	global_load_dwordx4 v[134:137], v[130:131], off offset:128
	s_nop 0
	global_load_dwordx4 v[130:133], v[130:131], off offset:144
	v_lshl_add_u32 v172, s64, 8, v159
	v_ashrrev_i32_e32 v173, 31, v172
	v_or_b32_e32 v174, 16, v172
	v_or_b32_e32 v176, 32, v172
	v_or_b32_e32 v178, 48, v172
	v_lshlrev_b64 v[172:173], 12, v[172:173]
	v_ashrrev_i32_e32 v175, 31, v174
	v_ashrrev_i32_e32 v177, 31, v176
	v_ashrrev_i32_e32 v179, 31, v178
	v_lshlrev_b64 v[180:181], 1, v[164:165]
	v_lshl_add_u64 v[164:165], s[12:13], 0, v[172:173]
	v_lshlrev_b64 v[172:173], 12, v[174:175]
	v_lshlrev_b64 v[174:175], 12, v[176:177]
	v_lshlrev_b64 v[176:177], 12, v[178:179]
	v_lshl_add_u64 v[172:173], s[12:13], 0, v[172:173]
	v_lshl_add_u64 v[174:175], s[12:13], 0, v[174:175]
	v_lshl_add_u64 v[176:177], s[12:13], 0, v[176:177]
	v_lshl_add_u64 v[164:165], v[164:165], 0, v[180:181]
	v_lshl_add_u64 v[172:173], v[172:173], 0, v[180:181]
	v_lshl_add_u64 v[174:175], v[174:175], 0, v[180:181]
	v_lshl_add_u64 v[176:177], v[176:177], 0, v[180:181]
	s_waitcnt vmcnt(0)
	v_pk_mul_f32 v[124:125], v[124:125], v[144:145]
	v_pk_mul_f32 v[122:123], v[122:123], v[142:143]
	v_pk_mul_f32 v[180:181], v[72:73], v[136:137]
	v_cvt_pk_bf16_f32 v72, v122, v123
	v_cvt_pk_bf16_f32 v73, v124, v125
	v_pk_mul_f32 v[128:129], v[128:129], v[140:141]
	v_pk_mul_f32 v[126:127], v[126:127], v[138:139]
	v_pk_mul_f32 v[120:121], v[120:121], v[136:137]
	v_pk_mul_f32 v[118:119], v[118:119], v[134:135]
	v_pk_mul_f32 v[178:179], v[74:75], v[138:139]
	v_cvt_pk_bf16_f32 v74, v126, v127
	v_cvt_pk_bf16_f32 v75, v128, v129
	global_store_dwordx4 v[164:165], v[72:75], off sc1
	v_pk_mul_f32 v[116:117], v[116:117], v[132:133]
	v_pk_mul_f32 v[114:115], v[114:115], v[130:131]
	v_cvt_pk_bf16_f32 v72, v118, v119
	v_cvt_pk_bf16_f32 v73, v120, v121
	v_pk_mul_f32 v[112:113], v[112:113], v[144:145]
	v_pk_mul_f32 v[110:111], v[110:111], v[142:143]
	v_cvt_pk_bf16_f32 v74, v114, v115
	v_cvt_pk_bf16_f32 v75, v116, v117
	global_store_dwordx4 v[164:165], v[72:75], off offset:64 sc1
	v_pk_mul_f32 v[108:109], v[108:109], v[140:141]
	v_pk_mul_f32 v[106:107], v[106:107], v[138:139]
	v_cvt_pk_bf16_f32 v72, v110, v111
	v_cvt_pk_bf16_f32 v73, v112, v113
	v_pk_mul_f32 v[104:105], v[104:105], v[136:137]
	v_pk_mul_f32 v[102:103], v[102:103], v[134:135]
	v_cvt_pk_bf16_f32 v74, v106, v107
	v_cvt_pk_bf16_f32 v75, v108, v109
	global_store_dwordx4 v[172:173], v[72:75], off sc1
	v_pk_mul_f32 v[100:101], v[100:101], v[132:133]
	v_pk_mul_f32 v[98:99], v[98:99], v[130:131]
	v_cvt_pk_bf16_f32 v72, v102, v103
	v_cvt_pk_bf16_f32 v73, v104, v105
	v_pk_mul_f32 v[96:97], v[96:97], v[144:145]
	v_pk_mul_f32 v[94:95], v[94:95], v[142:143]
	v_cvt_pk_bf16_f32 v74, v98, v99
	v_cvt_pk_bf16_f32 v75, v100, v101
	global_store_dwordx4 v[172:173], v[72:75], off offset:64 sc1
	v_pk_mul_f32 v[92:93], v[92:93], v[140:141]
	v_pk_mul_f32 v[90:91], v[90:91], v[138:139]
	v_cvt_pk_bf16_f32 v72, v94, v95
	v_cvt_pk_bf16_f32 v73, v96, v97
	v_pk_mul_f32 v[88:89], v[88:89], v[136:137]
	v_pk_mul_f32 v[86:87], v[86:87], v[134:135]
	v_cvt_pk_bf16_f32 v74, v90, v91
	v_cvt_pk_bf16_f32 v75, v92, v93
	global_store_dwordx4 v[174:175], v[72:75], off sc1
	v_pk_mul_f32 v[84:85], v[84:85], v[132:133]
	v_pk_mul_f32 v[82:83], v[82:83], v[130:131]
	v_cvt_pk_bf16_f32 v72, v86, v87
	v_cvt_pk_bf16_f32 v73, v88, v89
	v_pk_mul_f32 v[80:81], v[80:81], v[144:145]
	v_pk_mul_f32 v[78:79], v[78:79], v[142:143]
	v_cvt_pk_bf16_f32 v74, v82, v83
	v_cvt_pk_bf16_f32 v75, v84, v85
	global_store_dwordx4 v[174:175], v[72:75], off offset:64 sc1
	v_pk_mul_f32 v[76:77], v[76:77], v[140:141]
	v_pk_mul_f32 v[70:71], v[70:71], v[134:135]
	v_cvt_pk_bf16_f32 v72, v78, v79
	v_cvt_pk_bf16_f32 v73, v80, v81
	v_cvt_pk_bf16_f32 v74, v178, v179
	v_cvt_pk_bf16_f32 v75, v76, v77
	global_store_dwordx4 v[176:177], v[72:75], off sc1
	v_pk_mul_f32 v[62:63], v[62:63], v[142:143]
	v_pk_mul_f32 v[64:65], v[64:65], v[144:145]
	v_pk_mul_f32 v[72:73], v[68:69], v[132:133]
	v_pk_mul_f32 v[68:69], v[66:67], v[130:131]
	v_cvt_pk_bf16_f32 v66, v70, v71
	v_cvt_pk_bf16_f32 v67, v180, v181
	v_pk_mul_f32 v[56:57], v[56:57], v[136:137]
	v_cvt_pk_bf16_f32 v68, v68, v69
	v_cvt_pk_bf16_f32 v69, v72, v73
	global_store_dwordx4 v[176:177], v[66:69], off offset:64 sc1
	v_pk_mul_f32 v[54:55], v[54:55], v[134:135]
	v_pk_mul_f32 v[46:47], v[46:47], v[142:143]
	v_pk_mul_f32 v[68:69], v[60:61], v[140:141]
	v_pk_mul_f32 v[60:61], v[58:59], v[138:139]
	v_cvt_pk_bf16_f32 v58, v62, v63
	v_add_co_u32_e32 v62, vcc, s59, v164
	v_cvt_pk_bf16_f32 v59, v64, v65
	v_cvt_pk_bf16_f32 v60, v60, v61
	v_cvt_pk_bf16_f32 v61, v68, v69
	v_lshl_add_u64 v[66:67], v[164:165], 0, s[24:25]
	s_nop 0
	v_addc_co_u32_e32 v63, vcc, 0, v165, vcc
	global_store_dwordx4 v[62:63], v[58:61], off sc1
	v_pk_mul_f32 v[48:49], v[48:49], v[144:145]
	v_pk_mul_f32 v[40:41], v[40:41], v[136:137]
	v_pk_mul_f32 v[58:59], v[52:53], v[132:133]
	v_pk_mul_f32 v[52:53], v[50:51], v[130:131]
	v_cvt_pk_bf16_f32 v50, v54, v55
	v_cvt_pk_bf16_f32 v51, v56, v57
	v_pk_mul_f32 v[38:39], v[38:39], v[134:135]
	v_cvt_pk_bf16_f32 v52, v52, v53
	v_cvt_pk_bf16_f32 v53, v58, v59
	global_store_dwordx4 v[66:67], v[50:53], off offset:64 sc1
	v_pk_mul_f32 v[30:31], v[30:31], v[142:143]
	v_pk_mul_f32 v[32:33], v[32:33], v[144:145]
	v_pk_mul_f32 v[52:53], v[44:45], v[140:141]
	v_pk_mul_f32 v[44:45], v[42:43], v[138:139]
	v_cvt_pk_bf16_f32 v42, v46, v47
	v_add_co_u32_e32 v46, vcc, s60, v164
	v_cvt_pk_bf16_f32 v43, v48, v49
	v_cvt_pk_bf16_f32 v44, v44, v45
	v_cvt_pk_bf16_f32 v45, v52, v53
	v_lshl_add_u64 v[50:51], v[164:165], 0, s[26:27]
	s_nop 0
	v_addc_co_u32_e32 v47, vcc, 0, v165, vcc
	global_store_dwordx4 v[46:47], v[42:45], off sc1
	v_pk_mul_f32 v[24:25], v[24:25], v[136:137]
	v_pk_mul_f32 v[22:23], v[22:23], v[134:135]
	v_pk_mul_f32 v[42:43], v[36:37], v[132:133]
	v_pk_mul_f32 v[36:37], v[34:35], v[130:131]
	v_cvt_pk_bf16_f32 v34, v38, v39
	v_cvt_pk_bf16_f32 v35, v40, v41
	v_pk_mul_f32 v[14:15], v[14:15], v[142:143]
	v_cvt_pk_bf16_f32 v36, v36, v37
	v_cvt_pk_bf16_f32 v37, v42, v43
	global_store_dwordx4 v[50:51], v[34:37], off offset:64 sc1
	v_pk_mul_f32 v[16:17], v[16:17], v[144:145]
	v_pk_mul_f32 v[8:9], v[8:9], v[136:137]
	v_pk_mul_f32 v[36:37], v[28:29], v[140:141]
	v_pk_mul_f32 v[28:29], v[26:27], v[138:139]
	v_cvt_pk_bf16_f32 v26, v30, v31
	v_add_co_u32_e32 v30, vcc, s61, v164
	v_cvt_pk_bf16_f32 v27, v32, v33
	v_cvt_pk_bf16_f32 v28, v28, v29
	v_cvt_pk_bf16_f32 v29, v36, v37
	v_lshl_add_u64 v[34:35], v[164:165], 0, s[28:29]
	s_nop 0
	v_addc_co_u32_e32 v31, vcc, 0, v165, vcc
	global_store_dwordx4 v[30:31], v[26:29], off sc1
	v_pk_mul_f32 v[6:7], v[6:7], v[134:135]
	s_nop 0
	v_pk_mul_f32 v[26:27], v[20:21], v[132:133]
	v_pk_mul_f32 v[20:21], v[18:19], v[130:131]
	v_cvt_pk_bf16_f32 v18, v22, v23
	v_cvt_pk_bf16_f32 v19, v24, v25
	s_nop 0
	v_cvt_pk_bf16_f32 v20, v20, v21
	v_cvt_pk_bf16_f32 v21, v26, v27
	global_store_dwordx4 v[34:35], v[18:21], off offset:64 sc1
	s_nop 1
	v_pk_mul_f32 v[20:21], v[12:13], v[140:141]
	v_pk_mul_f32 v[12:13], v[10:11], v[138:139]
	v_cvt_pk_bf16_f32 v10, v14, v15
	v_add_co_u32_e32 v14, vcc, s62, v164
	v_cvt_pk_bf16_f32 v11, v16, v17
	v_lshl_add_u64 v[18:19], v[164:165], 0, s[30:31]
	s_nop 0
	v_addc_co_u32_e32 v15, vcc, 0, v165, vcc
	v_cvt_pk_bf16_f32 v12, v12, v13
	v_cvt_pk_bf16_f32 v13, v20, v21
	global_store_dwordx4 v[14:15], v[10:13], off sc1
	s_and_b64 vcc, exec, s[0:1]
	s_mov_b64 s[0:1], -1
	v_pk_mul_f32 v[10:11], v[4:5], v[132:133]
	v_pk_mul_f32 v[4:5], v[2:3], v[130:131]
	v_cvt_pk_bf16_f32 v2, v6, v7
	v_cvt_pk_bf16_f32 v3, v8, v9
	s_nop 0
	v_cvt_pk_bf16_f32 v4, v4, v5
	v_cvt_pk_bf16_f32 v5, v10, v11
	global_store_dwordx4 v[18:19], v[2:5], off offset:64 sc1
	s_mov_b32 s100, 1
	s_cbranch_vccnz .LBB0_1063
	s_andn2_b64 vcc, exec, s[10:11]
	s_cbranch_vccnz .LBB0_1062
	s_barrier
	s_branch .LBB0_1062
